# grid barrier: last-arriving XCD leader releases all per-XCD generation words itself (one hop less on release path), on top of v028
# speedup vs baseline: 1.0063x; 1.0063x over previous
; __device__ __forceinline__ unsigned xb_ld(unsigned* p)              { return __hip_atomic_load(p, __ATOMIC_RELAXED, __HIP_MEMORY_SCOPE_AGENT); }
; __device__ __forceinline__ unsigned xb_add(unsigned* p, unsigned v) { return __hip_atomic_fetch_add(p, v, __ATOMIC_RELAXED, __HIP_MEMORY_SCOPE_AGENT); }
; #define XB_SPIN(cond, bar) do { unsigned _sp = 0; while (cond) { __builtin_amdgcn_s_sleep(1); \
;     if ((++_sp & 255u) == 0u) { if (xb_ld(&(bar)[XB_TMO])) break; if (_sp > XB_SPIN_CAP) { atomicAdd(&(bar)[XB_TMO], 1u); break; } } } } while (0)
; __device__ __forceinline__ void xcd_barrier(const XcdBarrier& b) {
;     ...
;             const unsigned og = xb_add(&bar[XB_TOP], 1u);
;             const unsigned tg = og / nx;
;             if (og + 1u == (tg + 1u) * nx) xb_add(&bar[XB_TOPGEN], 1u);
;             else XB_SPIN(xb_ld(&bar[XB_TOPGEN]) == tg, bar);
;             __builtin_amdgcn_fence(__ATOMIC_ACQUIRE, "agent");
;             xb_add(&bar[XB_XGEN(b.x)], 1u);
.LBB0_318:
	s_or_b64 exec, exec, s[8:9]
	s_waitcnt vmcnt(0)
	v_readfirstlane_b32 s5, v3
	v_sub_u32_e32 v4, 0, v2
	v_readlane_b32 s6, v253, 52
	v_add_u32_e32 v3, s5, v1
	v_cvt_f32_u32_e32 v1, v2
	v_readlane_b32 s7, v253, 53
	s_mov_b64 s[8:9], -1
	v_rcp_iflag_f32_e32 v1, v1
	s_nop 0
	v_mul_f32_e32 v1, 0x4f7ffffe, v1
	v_cvt_u32_f32_e32 v1, v1
	v_mul_lo_u32 v4, v4, v1
	v_mul_hi_u32 v4, v1, v4
	v_add_u32_e32 v1, v1, v4
	v_mul_hi_u32 v1, v3, v1
	v_mul_lo_u32 v4, v1, v2
	v_sub_u32_e32 v4, v3, v4
	v_cmp_ge_u32_e32 vcc, v4, v2
	v_add_u32_e32 v5, 1, v1
	v_add_u32_e32 v3, 1, v3
	v_cndmask_b32_e32 v1, v1, v5, vcc
	v_sub_u32_e32 v5, v4, v2
	v_cndmask_b32_e32 v4, v4, v5, vcc
	v_cmp_ge_u32_e32 vcc, v4, v2
	v_add_u32_e32 v4, 1, v1
	s_nop 0
	v_cndmask_b32_e32 v1, v1, v4, vcc
	v_mul_lo_u32 v4, v2, v1
	v_add_u32_e32 v2, v4, v2
	v_cmp_ne_u32_e32 vcc, v3, v2
	v_mov_b64_e32 v[2:3], s[6:7]
	s_cbranch_vccnz .Lbar_notlast_0
	s_add_u32 s98, s6, 0xffffef00
	s_addc_u32 s99, s7, -1
	global_atomic_add v163, v197, s[98:99]
	global_atomic_add v163, v197, s[98:99] offset:256
	global_atomic_add v163, v197, s[98:99] offset:512
	global_atomic_add v163, v197, s[98:99] offset:768
	global_atomic_add v163, v197, s[98:99] offset:1024
	global_atomic_add v163, v197, s[98:99] offset:1280
	global_atomic_add v163, v197, s[98:99] offset:1536
	global_atomic_add v163, v197, s[98:99] offset:1792
	global_atomic_add v163, v197, s[98:99] offset:2048
	global_atomic_add v163, v197, s[98:99] offset:2304
	global_atomic_add v163, v197, s[98:99] offset:2560
	global_atomic_add v163, v197, s[98:99] offset:2816
	global_atomic_add v163, v197, s[98:99] offset:3072
	global_atomic_add v163, v197, s[98:99] offset:3328
	global_atomic_add v163, v197, s[98:99] offset:3584
	global_atomic_add v163, v197, s[98:99] offset:3840
.Lbar_notlast_0:
	s_and_saveexec_b64 s[6:7], vcc
	s_cbranch_execz .LBB0_330
	v_readlane_b32 s8, v253, 52
	v_readlane_b32 s9, v253, 53
	s_mov_b64 s[12:13], 0
	s_nop 3
	global_load_dword v2, v163, s[8:9] sc1
	s_waitcnt vmcnt(0)
	v_cmp_eq_u32_e32 vcc, v2, v1
	s_and_saveexec_b64 s[8:9], vcc
	s_cbranch_execz .LBB0_329
	s_mov_b32 s5, 1
	s_branch .LBB0_322

; __device__ __forceinline__ unsigned xb_ld(unsigned* p)              { return __hip_atomic_load(p, __ATOMIC_RELAXED, __HIP_MEMORY_SCOPE_AGENT); }
; __device__ __forceinline__ unsigned xb_add(unsigned* p, unsigned v) { return __hip_atomic_fetch_add(p, v, __ATOMIC_RELAXED, __HIP_MEMORY_SCOPE_AGENT); }
; #define XB_SPIN(cond, bar) do { unsigned _sp = 0; while (cond) { __builtin_amdgcn_s_sleep(1); \
;     if ((++_sp & 255u) == 0u) { if (xb_ld(&(bar)[XB_TMO])) break; if (_sp > XB_SPIN_CAP) { atomicAdd(&(bar)[XB_TMO], 1u); break; } } } } while (0)
; __device__ __forceinline__ void xcd_barrier(const XcdBarrier& b) {
;     ...
;             else XB_SPIN(xb_ld(&bar[XB_TOPGEN]) == tg, bar);
;             __builtin_amdgcn_fence(__ATOMIC_ACQUIRE, "agent");
;             xb_add(&bar[XB_XGEN(b.x)], 1u);
;             asm volatile("s_waitcnt vmcnt(0)" ::: "memory");
.LBB0_332:
	s_or_b64 exec, exec, s[6:7]
	s_mov_b64 s[6:7], exec
	v_mbcnt_lo_u32_b32 v1, s6, 0
	v_mbcnt_hi_u32_b32 v1, s7, v1
	v_cmp_eq_u32_e32 vcc, 0, v1
	s_waitcnt vmcnt(0)
	s_and_saveexec_b64 s[8:9], vcc
	s_cbranch_execz .LBB0_334
	s_bcnt1_i32_b64 s5, s[6:7]
	v_readlane_b32 s6, v253, 48
	v_mov_b32_e32 v1, s5
	v_readlane_b32 s7, v253, 49
	s_nop 4
.LBB0_334:
	s_or_b64 exec, exec, s[8:9]
	s_waitcnt vmcnt(0)

; __device__ __forceinline__ unsigned xb_ld(unsigned* p)              { return __hip_atomic_load(p, __ATOMIC_RELAXED, __HIP_MEMORY_SCOPE_AGENT); }
; __device__ __forceinline__ unsigned xb_add(unsigned* p, unsigned v) { return __hip_atomic_fetch_add(p, v, __ATOMIC_RELAXED, __HIP_MEMORY_SCOPE_AGENT); }
; #define XB_SPIN(cond, bar) do { unsigned _sp = 0; while (cond) { __builtin_amdgcn_s_sleep(1); \
;     if ((++_sp & 255u) == 0u) { if (xb_ld(&(bar)[XB_TMO])) break; if (_sp > XB_SPIN_CAP) { atomicAdd(&(bar)[XB_TMO], 1u); break; } } } } while (0)
; __device__ __forceinline__ void xcd_barrier(const XcdBarrier& b) {
;     ...
;             else XB_SPIN(xb_ld(&bar[XB_TOPGEN]) == tg, bar);
;             __builtin_amdgcn_fence(__ATOMIC_ACQUIRE, "agent");
;             xb_add(&bar[XB_XGEN(b.x)], 1u);
;             asm volatile("s_waitcnt vmcnt(0)" ::: "memory");
.LBB0_409:
	s_or_b64 exec, exec, s[6:7]
	s_mov_b64 s[6:7], exec
	v_mbcnt_lo_u32_b32 v1, s6, 0
	v_mbcnt_hi_u32_b32 v1, s7, v1
	v_cmp_eq_u32_e32 vcc, 0, v1
	s_waitcnt vmcnt(0)
	s_and_saveexec_b64 s[8:9], vcc
	s_cbranch_execz .LBB0_411
	s_bcnt1_i32_b64 s5, s[6:7]
	v_readlane_b32 s6, v253, 48
	v_mov_b32_e32 v1, s5
	v_readlane_b32 s7, v253, 49
	s_nop 4
.LBB0_411:
	s_or_b64 exec, exec, s[8:9]
	s_waitcnt vmcnt(0)

; __device__ __forceinline__ unsigned xb_ld(unsigned* p)              { return __hip_atomic_load(p, __ATOMIC_RELAXED, __HIP_MEMORY_SCOPE_AGENT); }
; __device__ __forceinline__ unsigned xb_add(unsigned* p, unsigned v) { return __hip_atomic_fetch_add(p, v, __ATOMIC_RELAXED, __HIP_MEMORY_SCOPE_AGENT); }
; #define XB_SPIN(cond, bar) do { unsigned _sp = 0; while (cond) { __builtin_amdgcn_s_sleep(1); \
;     if ((++_sp & 255u) == 0u) { if (xb_ld(&(bar)[XB_TMO])) break; if (_sp > XB_SPIN_CAP) { atomicAdd(&(bar)[XB_TMO], 1u); break; } } } } while (0)
; __device__ __forceinline__ void xcd_barrier(const XcdBarrier& b) {
;     ...
;             else XB_SPIN(xb_ld(&bar[XB_TOPGEN]) == tg, bar);
;             __builtin_amdgcn_fence(__ATOMIC_ACQUIRE, "agent");
;             xb_add(&bar[XB_XGEN(b.x)], 1u);
;             asm volatile("s_waitcnt vmcnt(0)" ::: "memory");
.LBB0_524:
	s_or_b64 exec, exec, s[6:7]
	s_mov_b64 s[6:7], exec
	v_mbcnt_lo_u32_b32 v1, s6, 0
	v_mbcnt_hi_u32_b32 v1, s7, v1
	v_cmp_eq_u32_e32 vcc, 0, v1
	s_waitcnt vmcnt(0)
	s_and_saveexec_b64 s[8:9], vcc
	s_cbranch_execz .LBB0_526
	s_bcnt1_i32_b64 s5, s[6:7]
	v_readlane_b32 s6, v253, 48
	v_mov_b32_e32 v1, s5
	v_readlane_b32 s7, v253, 49
	s_nop 4
.LBB0_526:
	s_or_b64 exec, exec, s[8:9]
	s_waitcnt vmcnt(0)

; __device__ __forceinline__ unsigned xb_ld(unsigned* p)              { return __hip_atomic_load(p, __ATOMIC_RELAXED, __HIP_MEMORY_SCOPE_AGENT); }
; __device__ __forceinline__ unsigned xb_add(unsigned* p, unsigned v) { return __hip_atomic_fetch_add(p, v, __ATOMIC_RELAXED, __HIP_MEMORY_SCOPE_AGENT); }
; #define XB_SPIN(cond, bar) do { unsigned _sp = 0; while (cond) { __builtin_amdgcn_s_sleep(1); \
;     if ((++_sp & 255u) == 0u) { if (xb_ld(&(bar)[XB_TMO])) break; if (_sp > XB_SPIN_CAP) { atomicAdd(&(bar)[XB_TMO], 1u); break; } } } } while (0)
; __device__ __forceinline__ void xcd_barrier(const XcdBarrier& b) {
;     ...
;             else XB_SPIN(xb_ld(&bar[XB_TOPGEN]) == tg, bar);
;             __builtin_amdgcn_fence(__ATOMIC_ACQUIRE, "agent");
;             xb_add(&bar[XB_XGEN(b.x)], 1u);
;             asm volatile("s_waitcnt vmcnt(0)" ::: "memory");
.LBB0_753:
	s_or_b64 exec, exec, s[6:7]
	s_mov_b64 s[6:7], exec
	v_mbcnt_lo_u32_b32 v1, s6, 0
	v_mbcnt_hi_u32_b32 v1, s7, v1
	v_cmp_eq_u32_e32 vcc, 0, v1
	s_waitcnt vmcnt(0)
	s_and_saveexec_b64 s[8:9], vcc
	s_cbranch_execz .LBB0_755
	s_bcnt1_i32_b64 s5, s[6:7]
	v_readlane_b32 s6, v253, 48
	v_mov_b32_e32 v1, s5
	v_readlane_b32 s7, v253, 49
	s_nop 4
.LBB0_755:
	s_or_b64 exec, exec, s[8:9]
	s_waitcnt vmcnt(0)

; __device__ __forceinline__ unsigned xb_ld(unsigned* p)              { return __hip_atomic_load(p, __ATOMIC_RELAXED, __HIP_MEMORY_SCOPE_AGENT); }
; __device__ __forceinline__ unsigned xb_add(unsigned* p, unsigned v) { return __hip_atomic_fetch_add(p, v, __ATOMIC_RELAXED, __HIP_MEMORY_SCOPE_AGENT); }
; #define XB_SPIN(cond, bar) do { unsigned _sp = 0; while (cond) { __builtin_amdgcn_s_sleep(1); \
;     if ((++_sp & 255u) == 0u) { if (xb_ld(&(bar)[XB_TMO])) break; if (_sp > XB_SPIN_CAP) { atomicAdd(&(bar)[XB_TMO], 1u); break; } } } } while (0)
; __device__ __forceinline__ void xcd_barrier(const XcdBarrier& b) {
;     ...
;             else XB_SPIN(xb_ld(&bar[XB_TOPGEN]) == tg, bar);
;             __builtin_amdgcn_fence(__ATOMIC_ACQUIRE, "agent");
;             xb_add(&bar[XB_XGEN(b.x)], 1u);
;             asm volatile("s_waitcnt vmcnt(0)" ::: "memory");
.LBB0_850:
	s_or_b64 exec, exec, s[6:7]
	s_mov_b64 s[6:7], exec
	v_mbcnt_lo_u32_b32 v1, s6, 0
	v_mbcnt_hi_u32_b32 v1, s7, v1
	v_cmp_eq_u32_e32 vcc, 0, v1
	s_waitcnt vmcnt(0)
	s_and_saveexec_b64 s[8:9], vcc
	s_cbranch_execz .LBB0_852
	s_bcnt1_i32_b64 s5, s[6:7]
	v_readlane_b32 s6, v253, 48
	v_mov_b32_e32 v1, s5
	v_readlane_b32 s7, v253, 49
	s_nop 4
.LBB0_852:
	s_or_b64 exec, exec, s[8:9]
	s_waitcnt vmcnt(0)

; __device__ __forceinline__ unsigned xb_ld(unsigned* p)              { return __hip_atomic_load(p, __ATOMIC_RELAXED, __HIP_MEMORY_SCOPE_AGENT); }
; __device__ __forceinline__ unsigned xb_add(unsigned* p, unsigned v) { return __hip_atomic_fetch_add(p, v, __ATOMIC_RELAXED, __HIP_MEMORY_SCOPE_AGENT); }
; #define XB_SPIN(cond, bar) do { unsigned _sp = 0; while (cond) { __builtin_amdgcn_s_sleep(1); \
;     if ((++_sp & 255u) == 0u) { if (xb_ld(&(bar)[XB_TMO])) break; if (_sp > XB_SPIN_CAP) { atomicAdd(&(bar)[XB_TMO], 1u); break; } } } } while (0)
; __device__ __forceinline__ void xcd_barrier(const XcdBarrier& b) {
;     ...
;             else XB_SPIN(xb_ld(&bar[XB_TOPGEN]) == tg, bar);
;             __builtin_amdgcn_fence(__ATOMIC_ACQUIRE, "agent");
;             xb_add(&bar[XB_XGEN(b.x)], 1u);
;             asm volatile("s_waitcnt vmcnt(0)" ::: "memory");
.LBB0_976:
	s_or_b64 exec, exec, s[6:7]
	s_mov_b64 s[6:7], exec
	v_mbcnt_lo_u32_b32 v1, s6, 0
	v_mbcnt_hi_u32_b32 v1, s7, v1
	v_cmp_eq_u32_e32 vcc, 0, v1
	s_waitcnt vmcnt(0)
	s_and_saveexec_b64 s[8:9], vcc
	s_cbranch_execz .LBB0_978
	s_bcnt1_i32_b64 s5, s[6:7]
	v_readlane_b32 s6, v253, 48
	v_mov_b32_e32 v1, s5
	v_readlane_b32 s7, v253, 49
	s_nop 4
.LBB0_978:
	s_or_b64 exec, exec, s[8:9]
	s_waitcnt vmcnt(0)

; __device__ __forceinline__ unsigned xb_ld(unsigned* p)              { return __hip_atomic_load(p, __ATOMIC_RELAXED, __HIP_MEMORY_SCOPE_AGENT); }
; __device__ __forceinline__ unsigned xb_add(unsigned* p, unsigned v) { return __hip_atomic_fetch_add(p, v, __ATOMIC_RELAXED, __HIP_MEMORY_SCOPE_AGENT); }
; #define XB_SPIN(cond, bar) do { unsigned _sp = 0; while (cond) { __builtin_amdgcn_s_sleep(1); \
;     if ((++_sp & 255u) == 0u) { if (xb_ld(&(bar)[XB_TMO])) break; if (_sp > XB_SPIN_CAP) { atomicAdd(&(bar)[XB_TMO], 1u); break; } } } } while (0)
; __device__ __forceinline__ void xcd_barrier(const XcdBarrier& b) {
;     ...
;             else XB_SPIN(xb_ld(&bar[XB_TOPGEN]) == tg, bar);
;             __builtin_amdgcn_fence(__ATOMIC_ACQUIRE, "agent");
;             xb_add(&bar[XB_XGEN(b.x)], 1u);
;             asm volatile("s_waitcnt vmcnt(0)" ::: "memory");
.LBB0_1036:
	s_or_b64 exec, exec, s[6:7]
	s_mov_b64 s[6:7], exec
	v_mbcnt_lo_u32_b32 v1, s6, 0
	v_mbcnt_hi_u32_b32 v1, s7, v1
	v_cmp_eq_u32_e32 vcc, 0, v1
	s_waitcnt vmcnt(0)
	s_and_saveexec_b64 s[8:9], vcc
	s_cbranch_execz .LBB0_1038
	s_bcnt1_i32_b64 s5, s[6:7]
	v_readlane_b32 s6, v253, 48
	v_mov_b32_e32 v1, s5
	v_readlane_b32 s7, v253, 49
	s_nop 4
.LBB0_1038:
	s_or_b64 exec, exec, s[8:9]
	s_waitcnt vmcnt(0)

; __device__ __forceinline__ unsigned xb_ld(unsigned* p)              { return __hip_atomic_load(p, __ATOMIC_RELAXED, __HIP_MEMORY_SCOPE_AGENT); }
; __device__ __forceinline__ unsigned xb_add(unsigned* p, unsigned v) { return __hip_atomic_fetch_add(p, v, __ATOMIC_RELAXED, __HIP_MEMORY_SCOPE_AGENT); }
; #define XB_SPIN(cond, bar) do { unsigned _sp = 0; while (cond) { __builtin_amdgcn_s_sleep(1); \
;     if ((++_sp & 255u) == 0u) { if (xb_ld(&(bar)[XB_TMO])) break; if (_sp > XB_SPIN_CAP) { atomicAdd(&(bar)[XB_TMO], 1u); break; } } } } while (0)
; __device__ __forceinline__ void xcd_barrier(const XcdBarrier& b) {
;     ...
;             else XB_SPIN(xb_ld(&bar[XB_TOPGEN]) == tg, bar);
;             __builtin_amdgcn_fence(__ATOMIC_ACQUIRE, "agent");
;             xb_add(&bar[XB_XGEN(b.x)], 1u);
;             asm volatile("s_waitcnt vmcnt(0)" ::: "memory");
.LBB0_1113:
	s_or_b64 exec, exec, s[6:7]
	s_mov_b64 s[6:7], exec
	v_mbcnt_lo_u32_b32 v1, s6, 0
	v_mbcnt_hi_u32_b32 v1, s7, v1
	v_cmp_eq_u32_e32 vcc, 0, v1
	s_waitcnt vmcnt(0)
	s_and_saveexec_b64 s[8:9], vcc
	s_cbranch_execz .LBB0_1115
	s_bcnt1_i32_b64 s5, s[6:7]
	v_readlane_b32 s6, v253, 48
	v_mov_b32_e32 v1, s5
	v_readlane_b32 s7, v253, 49
	s_nop 4
.LBB0_1115:
	s_or_b64 exec, exec, s[8:9]
	s_waitcnt vmcnt(0)

; __device__ __forceinline__ unsigned xb_ld(unsigned* p)              { return __hip_atomic_load(p, __ATOMIC_RELAXED, __HIP_MEMORY_SCOPE_AGENT); }
; __device__ __forceinline__ unsigned xb_add(unsigned* p, unsigned v) { return __hip_atomic_fetch_add(p, v, __ATOMIC_RELAXED, __HIP_MEMORY_SCOPE_AGENT); }
; #define XB_SPIN(cond, bar) do { unsigned _sp = 0; while (cond) { __builtin_amdgcn_s_sleep(1); \
;     if ((++_sp & 255u) == 0u) { if (xb_ld(&(bar)[XB_TMO])) break; if (_sp > XB_SPIN_CAP) { atomicAdd(&(bar)[XB_TMO], 1u); break; } } } } while (0)
; __device__ __forceinline__ void xcd_barrier(const XcdBarrier& b) {
;     ...
;             else XB_SPIN(xb_ld(&bar[XB_TOPGEN]) == tg, bar);
;             __builtin_amdgcn_fence(__ATOMIC_ACQUIRE, "agent");
;             xb_add(&bar[XB_XGEN(b.x)], 1u);
;             asm volatile("s_waitcnt vmcnt(0)" ::: "memory");
.LBB0_1189:
	s_or_b64 exec, exec, s[6:7]
	s_mov_b64 s[6:7], exec
	v_mbcnt_lo_u32_b32 v1, s6, 0
	v_mbcnt_hi_u32_b32 v1, s7, v1
	v_cmp_eq_u32_e32 vcc, 0, v1
	s_waitcnt vmcnt(0)
	s_and_saveexec_b64 s[8:9], vcc
	s_cbranch_execz .LBB0_1191
	s_bcnt1_i32_b64 s5, s[6:7]
	v_readlane_b32 s6, v253, 48
	v_mov_b32_e32 v1, s5
	v_readlane_b32 s7, v253, 49
	s_nop 4
.LBB0_1191:
	s_or_b64 exec, exec, s[8:9]
	s_waitcnt vmcnt(0)

; __device__ __forceinline__ unsigned xb_ld(unsigned* p)              { return __hip_atomic_load(p, __ATOMIC_RELAXED, __HIP_MEMORY_SCOPE_AGENT); }
; __device__ __forceinline__ unsigned xb_add(unsigned* p, unsigned v) { return __hip_atomic_fetch_add(p, v, __ATOMIC_RELAXED, __HIP_MEMORY_SCOPE_AGENT); }
; #define XB_SPIN(cond, bar) do { unsigned _sp = 0; while (cond) { __builtin_amdgcn_s_sleep(1); \
;     if ((++_sp & 255u) == 0u) { if (xb_ld(&(bar)[XB_TMO])) break; if (_sp > XB_SPIN_CAP) { atomicAdd(&(bar)[XB_TMO], 1u); break; } } } } while (0)
; __device__ __forceinline__ void xcd_barrier(const XcdBarrier& b) {
;     ...
;             else XB_SPIN(xb_ld(&bar[XB_TOPGEN]) == tg, bar);
;             __builtin_amdgcn_fence(__ATOMIC_ACQUIRE, "agent");
;             xb_add(&bar[XB_XGEN(b.x)], 1u);
;             asm volatile("s_waitcnt vmcnt(0)" ::: "memory");
.LBB0_1311:
	s_or_b64 exec, exec, s[6:7]
	s_mov_b64 s[6:7], exec
	v_mbcnt_lo_u32_b32 v1, s6, 0
	v_mbcnt_hi_u32_b32 v1, s7, v1
	v_cmp_eq_u32_e32 vcc, 0, v1
	s_waitcnt vmcnt(0)
	s_and_saveexec_b64 s[8:9], vcc
	s_cbranch_execz .LBB0_1313
	s_bcnt1_i32_b64 s5, s[6:7]
	v_readlane_b32 s6, v253, 48
	v_mov_b32_e32 v1, s5
	v_readlane_b32 s7, v253, 49
	s_nop 4
.LBB0_1313:
	s_or_b64 exec, exec, s[8:9]
	s_waitcnt vmcnt(0)

; __device__ __forceinline__ unsigned xb_ld(unsigned* p)              { return __hip_atomic_load(p, __ATOMIC_RELAXED, __HIP_MEMORY_SCOPE_AGENT); }
; __device__ __forceinline__ unsigned xb_add(unsigned* p, unsigned v) { return __hip_atomic_fetch_add(p, v, __ATOMIC_RELAXED, __HIP_MEMORY_SCOPE_AGENT); }
; #define XB_SPIN(cond, bar) do { unsigned _sp = 0; while (cond) { __builtin_amdgcn_s_sleep(1); \
;     if ((++_sp & 255u) == 0u) { if (xb_ld(&(bar)[XB_TMO])) break; if (_sp > XB_SPIN_CAP) { atomicAdd(&(bar)[XB_TMO], 1u); break; } } } } while (0)
; __device__ __forceinline__ void xcd_barrier(const XcdBarrier& b) {
;     ...
;             else XB_SPIN(xb_ld(&bar[XB_TOPGEN]) == tg, bar);
;             __builtin_amdgcn_fence(__ATOMIC_ACQUIRE, "agent");
;             xb_add(&bar[XB_XGEN(b.x)], 1u);
;             asm volatile("s_waitcnt vmcnt(0)" ::: "memory");
.LBB0_1432:
	s_or_b64 exec, exec, s[6:7]
	s_mov_b64 s[6:7], exec
	v_mbcnt_lo_u32_b32 v1, s6, 0
	v_mbcnt_hi_u32_b32 v1, s7, v1
	v_cmp_eq_u32_e32 vcc, 0, v1
	s_waitcnt vmcnt(0)
	s_and_saveexec_b64 s[8:9], vcc
	s_cbranch_execz .LBB0_1434
	s_bcnt1_i32_b64 s5, s[6:7]
	v_readlane_b32 s6, v253, 48
	v_mov_b32_e32 v1, s5
	v_readlane_b32 s7, v253, 49
	s_nop 4
.LBB0_1434:
	s_or_b64 exec, exec, s[8:9]
	s_waitcnt vmcnt(0)

; __device__ __forceinline__ unsigned xb_ld(unsigned* p)              { return __hip_atomic_load(p, __ATOMIC_RELAXED, __HIP_MEMORY_SCOPE_AGENT); }
; __device__ __forceinline__ unsigned xb_add(unsigned* p, unsigned v) { return __hip_atomic_fetch_add(p, v, __ATOMIC_RELAXED, __HIP_MEMORY_SCOPE_AGENT); }
; #define XB_SPIN(cond, bar) do { unsigned _sp = 0; while (cond) { __builtin_amdgcn_s_sleep(1); \
;     if ((++_sp & 255u) == 0u) { if (xb_ld(&(bar)[XB_TMO])) break; if (_sp > XB_SPIN_CAP) { atomicAdd(&(bar)[XB_TMO], 1u); break; } } } } while (0)
; __device__ __forceinline__ void xcd_barrier(const XcdBarrier& b) {
;     ...
;             else XB_SPIN(xb_ld(&bar[XB_TOPGEN]) == tg, bar);
;             __builtin_amdgcn_fence(__ATOMIC_ACQUIRE, "agent");
;             xb_add(&bar[XB_XGEN(b.x)], 1u);
;             asm volatile("s_waitcnt vmcnt(0)" ::: "memory");
.LBB0_1494:
	s_or_b64 exec, exec, s[6:7]
	s_mov_b64 s[6:7], exec
	v_mbcnt_lo_u32_b32 v1, s6, 0
	v_mbcnt_hi_u32_b32 v1, s7, v1
	v_cmp_eq_u32_e32 vcc, 0, v1
	s_waitcnt vmcnt(0)
	s_and_saveexec_b64 s[8:9], vcc
	s_cbranch_execz .LBB0_1496
	s_bcnt1_i32_b64 s5, s[6:7]
	v_readlane_b32 s6, v253, 48
	v_mov_b32_e32 v1, s5
	v_readlane_b32 s7, v253, 49
	s_nop 4
.LBB0_1496:
	s_or_b64 exec, exec, s[8:9]
	s_waitcnt vmcnt(0)

; __device__ __forceinline__ unsigned xb_ld(unsigned* p)              { return __hip_atomic_load(p, __ATOMIC_RELAXED, __HIP_MEMORY_SCOPE_AGENT); }
; __device__ __forceinline__ unsigned xb_add(unsigned* p, unsigned v) { return __hip_atomic_fetch_add(p, v, __ATOMIC_RELAXED, __HIP_MEMORY_SCOPE_AGENT); }
; #define XB_SPIN(cond, bar) do { unsigned _sp = 0; while (cond) { __builtin_amdgcn_s_sleep(1); \
;     if ((++_sp & 255u) == 0u) { if (xb_ld(&(bar)[XB_TMO])) break; if (_sp > XB_SPIN_CAP) { atomicAdd(&(bar)[XB_TMO], 1u); break; } } } } while (0)
; __device__ __forceinline__ void xcd_barrier(const XcdBarrier& b) {
;     ...
;             const unsigned og = xb_add(&bar[XB_TOP], 1u);
;             const unsigned tg = og / nx;
;             if (og + 1u == (tg + 1u) * nx) xb_add(&bar[XB_TOPGEN], 1u);
;             else XB_SPIN(xb_ld(&bar[XB_TOPGEN]) == tg, bar);
;             __builtin_amdgcn_fence(__ATOMIC_ACQUIRE, "agent");
;             xb_add(&bar[XB_XGEN(b.x)], 1u);
.LBB0_1555:
	s_or_b64 exec, exec, s[8:9]
	s_waitcnt vmcnt(0)
	v_readfirstlane_b32 s4, v3
	v_sub_u32_e32 v4, 0, v2
	s_mov_b64 s[8:9], -1
	v_add_u32_e32 v3, s4, v1
	v_cvt_f32_u32_e32 v1, v2
	v_readlane_b32 s4, v253, 52
	v_readlane_b32 s5, v253, 53
	v_rcp_iflag_f32_e32 v1, v1
	s_nop 0
	v_mul_f32_e32 v1, 0x4f7ffffe, v1
	v_cvt_u32_f32_e32 v1, v1
	v_mul_lo_u32 v4, v4, v1
	v_mul_hi_u32 v4, v1, v4
	v_add_u32_e32 v1, v1, v4
	v_mul_hi_u32 v1, v3, v1
	v_mul_lo_u32 v4, v1, v2
	v_sub_u32_e32 v4, v3, v4
	v_cmp_ge_u32_e32 vcc, v4, v2
	v_add_u32_e32 v5, 1, v1
	v_add_u32_e32 v3, 1, v3
	v_cndmask_b32_e32 v1, v1, v5, vcc
	v_sub_u32_e32 v5, v4, v2
	v_cndmask_b32_e32 v4, v4, v5, vcc
	v_cmp_ge_u32_e32 vcc, v4, v2
	v_add_u32_e32 v4, 1, v1
	s_nop 0
	v_cndmask_b32_e32 v1, v1, v4, vcc
	v_mul_lo_u32 v4, v2, v1
	v_add_u32_e32 v2, v4, v2
	v_cmp_ne_u32_e32 vcc, v3, v2
	v_mov_b64_e32 v[2:3], s[4:5]
	s_cbranch_vccnz .Lbar_notlast_12
	s_add_u32 s98, s4, 0xffffef00
	s_addc_u32 s99, s5, -1
	global_atomic_add v163, v197, s[98:99]
	global_atomic_add v163, v197, s[98:99] offset:256
	global_atomic_add v163, v197, s[98:99] offset:512
	global_atomic_add v163, v197, s[98:99] offset:768
	global_atomic_add v163, v197, s[98:99] offset:1024
	global_atomic_add v163, v197, s[98:99] offset:1280
	global_atomic_add v163, v197, s[98:99] offset:1536
	global_atomic_add v163, v197, s[98:99] offset:1792
	global_atomic_add v163, v197, s[98:99] offset:2048
	global_atomic_add v163, v197, s[98:99] offset:2304
	global_atomic_add v163, v197, s[98:99] offset:2560
	global_atomic_add v163, v197, s[98:99] offset:2816
	global_atomic_add v163, v197, s[98:99] offset:3072
	global_atomic_add v163, v197, s[98:99] offset:3328
	global_atomic_add v163, v197, s[98:99] offset:3584
	global_atomic_add v163, v197, s[98:99] offset:3840
.Lbar_notlast_12:
	s_and_saveexec_b64 s[6:7], vcc
	s_cbranch_execz .LBB0_1567
	v_readlane_b32 s4, v253, 52
	v_readlane_b32 s5, v253, 53
	s_mov_b64 s[12:13], 0
	s_nop 3
	global_load_dword v2, v163, s[4:5] sc1
	s_waitcnt vmcnt(0)
	v_cmp_eq_u32_e32 vcc, v2, v1
	s_and_saveexec_b64 s[8:9], vcc
	s_cbranch_execz .LBB0_1566
	s_mov_b32 s4, 1
	s_branch .LBB0_1559

; __device__ __forceinline__ unsigned xb_ld(unsigned* p)              { return __hip_atomic_load(p, __ATOMIC_RELAXED, __HIP_MEMORY_SCOPE_AGENT); }
; __device__ __forceinline__ unsigned xb_add(unsigned* p, unsigned v) { return __hip_atomic_fetch_add(p, v, __ATOMIC_RELAXED, __HIP_MEMORY_SCOPE_AGENT); }
; #define XB_SPIN(cond, bar) do { unsigned _sp = 0; while (cond) { __builtin_amdgcn_s_sleep(1); \
;     if ((++_sp & 255u) == 0u) { if (xb_ld(&(bar)[XB_TMO])) break; if (_sp > XB_SPIN_CAP) { atomicAdd(&(bar)[XB_TMO], 1u); break; } } } } while (0)
; __device__ __forceinline__ void xcd_barrier(const XcdBarrier& b) {
;     ...
;             else XB_SPIN(xb_ld(&bar[XB_TOPGEN]) == tg, bar);
;             __builtin_amdgcn_fence(__ATOMIC_ACQUIRE, "agent");
;             xb_add(&bar[XB_XGEN(b.x)], 1u);
;             asm volatile("s_waitcnt vmcnt(0)" ::: "memory");
.LBB0_1570:
	s_bcnt1_i32_b64 s4, s[6:7]
	v_mov_b32_e32 v1, s4
	v_readlane_b32 s4, v253, 48
	v_readlane_b32 s5, v253, 49
	s_nop 4
	s_getpc_b64 s[98:99]
